# speedup vs baseline: 1.0385x; 1.0108x over previous
.LBB0_15:
	s_load_dwordx4 s[4:7], s[0:1], 0x0
	s_load_dwordx2 s[10:11], s[0:1], 0x10
	s_lshl_b32 s0, s2, 8
	s_and_b32 s0, s0, 0x700
	s_add_i32 s0, s0, s2
	s_and_b32 s0, s0, 0x3ffff80
	s_and_b32 s1, s2, 0x60
	v_and_b32_e32 v2, 31, v0
	s_or_b32 s0, s1, s0
	v_lshrrev_b32_e32 v1, 6, v0
	v_lshrrev_b32_e32 v92, 6, v0
	v_mov_b32_e32 v93, 0
	v_and_b32_e32 v94, 63, v0
	v_lshlrev_b32_e32 v94, 4, v94
	v_lshl_add_u32 v95, v92, 10, v94
	v_bfe_u32 v38, v0, 5, 1
	v_or_b32_e32 v0, s0, v2
	s_lshr_b32 s0, s2, 1
	s_and_b32 s0, s0, 12
	v_or_b32_e32 v44, s0, v1
	v_lshlrev_b32_e32 v34, 6, v0
	v_bitop3_b32 v39, s0, 7, v1 bitop3:0xc8
	v_and_or_b32 v1, v44, 8, v38
	v_ashrrev_i32_e32 v35, 31, v34
	v_lshlrev_b32_e32 v45, 5, v39
	v_lshlrev_b32_e32 v3, 11, v1
	s_waitcnt lgkmcnt(0)
	v_lshl_add_u64 v[0:1], v[34:35], 2, s[4:5]
	v_lshlrev_b32_e32 v32, 5, v38
	v_mov_b32_e32 v33, 0
	v_lshl_add_u64 v[36:37], v[0:1], 0, v[32:33]
	v_or3_b32 v0, v45, v3, v2
	v_lshlrev_b32_e32 v0, 2, v0
	v_or_b32_e32 v1, 0x1000, v0
	v_or_b32_e32 v2, 0x1400, v0
	v_or_b32_e32 v3, 0x1800, v0
	v_or_b32_e32 v4, 0x1c00, v0
	v_lshlrev_b32_e32 v92, 6, v92
	v_lshl_add_u64 v[90:91], v[92:93], 0, v[36:37]
	global_load_dwordx4 v[28:31], v[90:91], off
	global_load_dwordx4 v[24:27], v[90:91], off offset:16
	global_load_dword v77, v0, s[6:7]
	global_load_dword v78, v0, s[6:7] offset:1024
	global_load_dword v79, v0, s[6:7] offset:2048
	global_load_dword v80, v0, s[6:7] offset:3072
	global_load_dword v81, v1, s[6:7]
	global_load_dword v82, v2, s[6:7]
	global_load_dword v83, v3, s[6:7]
	global_load_dword v84, v4, s[6:7]
	v_or_b32_e32 v1, 0x4000, v0
	v_or_b32_e32 v2, 0x4400, v0
	v_or_b32_e32 v3, 0x4800, v0
	v_or_b32_e32 v4, 0x4c00, v0
	v_or_b32_e32 v5, 0x5000, v0
	v_or_b32_e32 v6, 0x5400, v0
	v_or_b32_e32 v7, 0x5800, v0
	v_or_b32_e32 v8, 0x5c00, v0
	global_load_dword v69, v1, s[6:7]
	global_load_dword v70, v2, s[6:7]
	global_load_dword v71, v3, s[6:7]
	global_load_dword v72, v4, s[6:7]
	global_load_dword v73, v5, s[6:7]
	global_load_dword v74, v6, s[6:7]
	global_load_dword v75, v7, s[6:7]
	global_load_dword v76, v8, s[6:7]
	v_or_b32_e32 v1, 0x8000, v0
	v_or_b32_e32 v2, 0x8400, v0
	v_or_b32_e32 v3, 0x8800, v0
	v_or_b32_e32 v4, 0x8c00, v0
	v_or_b32_e32 v5, 0x9000, v0
	v_or_b32_e32 v6, 0x9400, v0
	v_or_b32_e32 v7, 0x9800, v0
	v_or_b32_e32 v8, 0x9c00, v0
	v_or_b32_e32 v46, 0xc000, v0
	global_load_dword v61, v1, s[6:7]
	global_load_dword v62, v2, s[6:7]
	global_load_dword v63, v3, s[6:7]
	global_load_dword v64, v4, s[6:7]
	global_load_dword v65, v5, s[6:7]
	global_load_dword v66, v6, s[6:7]
	global_load_dword v67, v7, s[6:7]
	global_load_dword v68, v8, s[6:7]
	v_or_b32_e32 v49, 0xc400, v0
	v_or_b32_e32 v50, 0xc800, v0
	v_or_b32_e32 v51, 0xcc00, v0
	v_or_b32_e32 v52, 0xd000, v0
	v_or_b32_e32 v53, 0xd400, v0
	v_or_b32_e32 v54, 0xd800, v0
	v_or_b32_e32 v55, 0xdc00, v0
	global_load_dword v32, v46, s[6:7]
	global_load_dword v35, v49, s[6:7]
	global_load_dword v40, v50, s[6:7]
	global_load_dword v41, v51, s[6:7]
	global_load_dword v42, v52, s[6:7]
	global_load_dword v43, v53, s[6:7]
	global_load_dword v47, v54, s[6:7]
	global_load_dword v48, v55, s[6:7]
	v_lshl_or_b32 v36, v38, 2, v45
	v_cmp_gt_u32_e32 vcc, 8, v44
	v_lshlrev_b32_e32 v85, 2, v36
	v_mov_b32_e32 v44, 0
	s_and_saveexec_b64 s[0:1], vcc
	s_cbranch_execz .LBB0_17
	global_load_dword v44, v85, s[10:11]

.LBB0_47:
	s_or_b64 exec, exec, s[0:1]
	s_waitcnt vmcnt(32)
	v_mul_f32_e32 v0, 0x3fb8aa3b, v28
	v_mul_f32_e32 v1, 0x3fb8aa3b, v29
	v_mul_f32_e32 v2, 0x3fb8aa3b, v30
	v_mul_f32_e32 v3, 0x3fb8aa3b, v31
	v_mul_f32_e32 v4, 0x3fb8aa3b, v24
	v_mul_f32_e32 v5, 0x3fb8aa3b, v25
	v_mul_f32_e32 v6, 0x3fb8aa3b, v26
	v_mul_f32_e32 v7, 0x3fb8aa3b, v27
	v_exp_f32_e32 v0, v0
	v_exp_f32_e32 v1, v1
	v_exp_f32_e32 v2, v2
	v_exp_f32_e32 v3, v3
	v_exp_f32_e32 v4, v4
	v_exp_f32_e32 v5, v5
	v_exp_f32_e32 v6, v6
	v_exp_f32_e32 v7, v7
	v_add_f32_e32 v0, -1.0, v0
	v_add_f32_e32 v1, -1.0, v1
	v_add_f32_e32 v2, -1.0, v2
	v_add_f32_e32 v3, -1.0, v3
	v_add_f32_e32 v4, -1.0, v4
	v_add_f32_e32 v5, -1.0, v5
	v_add_f32_e32 v6, -1.0, v6
	v_add_f32_e32 v7, -1.0, v7
	v_cmp_lt_f32_e64 s[0:1], 0, v28
	v_cmp_lt_f32_e64 s[2:3], 0, v29
	v_cmp_lt_f32_e64 s[4:5], 0, v30
	v_cmp_lt_f32_e64 s[6:7], 0, v31
	v_cndmask_b32_e64 v8, v0, v28, s[0:1]
	v_cndmask_b32_e64 v9, v1, v29, s[2:3]
	v_cndmask_b32_e64 v10, v2, v30, s[4:5]
	v_cndmask_b32_e64 v11, v3, v31, s[6:7]
	v_cmp_lt_f32_e64 s[0:1], 0, v24
	v_cmp_lt_f32_e64 s[2:3], 0, v25
	v_cmp_lt_f32_e64 s[4:5], 0, v26
	v_cmp_lt_f32_e64 s[6:7], 0, v27
	v_cndmask_b32_e64 v12, v4, v24, s[0:1]
	v_cndmask_b32_e64 v13, v5, v25, s[2:3]
	v_cndmask_b32_e64 v14, v6, v26, s[4:5]
	v_cndmask_b32_e64 v15, v7, v27, s[6:7]
	v_mul_f32_e32 v0, 0x3fb8aa3b, v8
	v_mul_f32_e32 v1, 0x3fb8aa3b, v9
	v_mul_f32_e32 v2, 0x3fb8aa3b, v10
	v_mul_f32_e32 v3, 0x3fb8aa3b, v11
	v_mul_f32_e32 v4, 0x3fb8aa3b, v12
	v_mul_f32_e32 v5, 0x3fb8aa3b, v13
	v_mul_f32_e32 v6, 0x3fb8aa3b, v14
	v_mul_f32_e32 v7, 0x3fb8aa3b, v15
	v_exp_f32_e32 v0, v0
	v_exp_f32_e32 v1, v1
	v_exp_f32_e32 v2, v2
	v_exp_f32_e32 v3, v3
	v_exp_f32_e32 v4, v4
	v_exp_f32_e32 v5, v5
	v_exp_f32_e32 v6, v6
	v_exp_f32_e32 v7, v7
	v_add_f32_e32 v0, -1.0, v0
	v_add_f32_e32 v1, -1.0, v1
	v_add_f32_e32 v2, -1.0, v2
	v_add_f32_e32 v3, -1.0, v3
	v_add_f32_e32 v4, -1.0, v4
	v_add_f32_e32 v5, -1.0, v5
	v_add_f32_e32 v6, -1.0, v6
	v_add_f32_e32 v7, -1.0, v7
	v_cmp_lt_f32_e64 s[0:1], 0, v8
	v_cmp_lt_f32_e64 s[2:3], 0, v9
	v_cmp_lt_f32_e64 s[4:5], 0, v10
	v_cmp_lt_f32_e64 s[6:7], 0, v11
	v_cndmask_b32_e64 v16, v0, v8, s[0:1]
	v_cndmask_b32_e64 v17, v1, v9, s[2:3]
	v_cndmask_b32_e64 v18, v2, v10, s[4:5]
	v_cndmask_b32_e64 v19, v3, v11, s[6:7]
	v_cmp_lt_f32_e64 s[0:1], 0, v12
	v_cmp_lt_f32_e64 s[2:3], 0, v13
	v_cmp_lt_f32_e64 s[4:5], 0, v14
	v_cmp_lt_f32_e64 s[6:7], 0, v15
	v_cndmask_b32_e64 v20, v4, v12, s[0:1]
	v_cndmask_b32_e64 v21, v5, v13, s[2:3]
	v_cndmask_b32_e64 v22, v6, v14, s[4:5]
	v_cndmask_b32_e64 v23, v7, v15, s[6:7]
	v_cvt_pk_f16_f32 v0, v16, v17
	v_cvt_pk_f16_f32 v1, v18, v19
	v_cvt_pk_f16_f32 v2, v20, v21
	v_cvt_pk_f16_f32 v3, v22, v23
	ds_write_b128 v95, v[0:3]
	s_waitcnt lgkmcnt(0)
	s_barrier
	ds_read_b128 v[0:3], v94
	ds_read_b128 v[4:7], v94 offset:1024
	ds_read_b128 v[8:11], v94 offset:2048
	ds_read_b128 v[12:15], v94 offset:3072
	s_waitcnt vmcnt(0)
	v_cvt_pk_f16_f32 v16, v77, v78
	v_cvt_pk_f16_f32 v17, v79, v80
	v_cvt_pk_f16_f32 v18, v81, v82
	v_cvt_pk_f16_f32 v19, v83, v84
	v_cvt_pk_f16_f32 v20, v69, v70
	v_cvt_pk_f16_f32 v21, v71, v72
	v_cvt_pk_f16_f32 v22, v73, v74
	v_cvt_pk_f16_f32 v23, v75, v76
	v_cvt_pk_f16_f32 v24, v61, v62
	v_cvt_pk_f16_f32 v25, v63, v64
	v_cvt_pk_f16_f32 v26, v65, v66
	v_cvt_pk_f16_f32 v27, v67, v68
	v_cvt_pk_f16_f32 v28, v32, v35
	v_cvt_pk_f16_f32 v29, v40, v41
	v_cvt_pk_f16_f32 v30, v42, v43
	v_cvt_pk_f16_f32 v31, v47, v48
	s_waitcnt lgkmcnt(0)
	v_mfma_f32_32x32x16_f16 a[0:15], v[16:19], v[0:3], 0
	v_mfma_f32_32x32x16_f16 a[0:15], v[20:23], v[4:7], a[0:15]
	v_mfma_f32_32x32x16_f16 a[0:15], v[24:27], v[8:11], a[0:15]
	v_mfma_f32_32x32x16_f16 a[0:15], v[28:31], v[12:15], a[0:15]
	v_lshlrev_b32_e32 v0, 3, v39
	v_or3_b32 v6, v0, v34, v38
	v_lshl_add_u64 v[4:5], s[8:9], 0, v[36:37]
	s_nop 9
	v_accvgpr_read_b32 v0, a0
	v_add_f32_e32 v0, v0, v44
	v_add_f32_e32 v1, 1.0, v0
	v_cndmask_b32_e32 v2, v0, v1, vcc
	v_mul_f32_e32 v0, 0x3fb8aa3b, v0
	v_exp_f32_e32 v7, v0
	v_accvgpr_read_b32 v0, a1
	v_add_f32_e32 v0, v0, v33
	v_add_f32_e32 v1, 1.0, v0
	v_cndmask_b32_e32 v3, v0, v1, vcc
	v_mul_f32_e32 v0, 0x3fb8aa3b, v0
	v_exp_f32_e32 v8, v0
	v_accvgpr_read_b32 v0, a2
	v_add_f32_e32 v0, v0, v50
	v_add_f32_e32 v1, 1.0, v0
	v_cndmask_b32_e32 v1, v0, v1, vcc
	v_mul_f32_e32 v0, 0x3fb8aa3b, v0
	v_exp_f32_e32 v9, v0
	v_accvgpr_read_b32 v0, a3
	v_add_f32_e32 v0, v0, v46
	v_mul_f32_e32 v11, 0x3fb8aa3b, v0
	v_exp_f32_e32 v11, v11
	v_add_f32_e32 v10, 1.0, v0
	v_cndmask_b32_e32 v0, v0, v10, vcc
	v_cvt_pk_f16_f32 v1, v1, v0
	v_cvt_pk_f16_f32 v0, v2, v3
	v_cvt_pk_f16_f32 v2, v7, v8
	v_ashrrev_i32_e32 v7, 31, v6
	v_cvt_pk_f16_f32 v3, v9, v11
	v_lshl_add_u64 v[4:5], v[6:7], 4, v[4:5]
	global_store_dwordx4 v[4:5], v[0:3], off
	s_nop 1
	v_accvgpr_read_b32 v0, a4
	v_add_f32_e32 v0, v0, v49
	v_add_f32_e32 v1, 1.0, v0
	v_cndmask_b32_e32 v2, v0, v1, vcc
	v_mul_f32_e32 v0, 0x3fb8aa3b, v0
	v_exp_f32_e32 v6, v0
	v_accvgpr_read_b32 v0, a5
	v_add_f32_e32 v0, v0, v45
	v_add_f32_e32 v1, 1.0, v0
	v_cndmask_b32_e32 v3, v0, v1, vcc
	v_mul_f32_e32 v0, 0x3fb8aa3b, v0
	v_exp_f32_e32 v7, v0
	v_accvgpr_read_b32 v0, a6
	v_add_f32_e32 v0, v0, v53
	v_add_f32_e32 v1, 1.0, v0
	v_cndmask_b32_e32 v1, v0, v1, vcc
	v_mul_f32_e32 v0, 0x3fb8aa3b, v0
	v_exp_f32_e32 v8, v0
	v_accvgpr_read_b32 v0, a7
	v_add_f32_e32 v0, v0, v51
	v_mul_f32_e32 v10, 0x3fb8aa3b, v0
	v_exp_f32_e32 v10, v10
	v_add_f32_e32 v9, 1.0, v0
	v_cndmask_b32_e32 v0, v0, v9, vcc
	v_cvt_pk_f16_f32 v1, v1, v0
	v_cvt_pk_f16_f32 v0, v2, v3
	v_cvt_pk_f16_f32 v3, v8, v10
	v_cvt_pk_f16_f32 v2, v6, v7
	global_store_dwordx4 v[4:5], v[0:3], off offset:32
	s_nop 1
	v_accvgpr_read_b32 v0, a8
	v_add_f32_e32 v0, v0, v54
	v_add_f32_e32 v1, 1.0, v0
	v_cndmask_b32_e32 v2, v0, v1, vcc
	v_mul_f32_e32 v0, 0x3fb8aa3b, v0
	v_exp_f32_e32 v6, v0
	v_accvgpr_read_b32 v0, a9
	v_add_f32_e32 v0, v0, v52
	v_add_f32_e32 v1, 1.0, v0
	v_cndmask_b32_e32 v3, v0, v1, vcc
	v_mul_f32_e32 v0, 0x3fb8aa3b, v0
	v_exp_f32_e32 v7, v0
	v_accvgpr_read_b32 v0, a10
	v_add_f32_e32 v0, v0, v57
	v_add_f32_e32 v1, 1.0, v0
	v_cndmask_b32_e32 v1, v0, v1, vcc
	v_mul_f32_e32 v0, 0x3fb8aa3b, v0
	v_exp_f32_e32 v8, v0
	v_accvgpr_read_b32 v0, a11
	v_add_f32_e32 v0, v0, v55
	v_mul_f32_e32 v10, 0x3fb8aa3b, v0
	v_exp_f32_e32 v10, v10
	v_add_f32_e32 v9, 1.0, v0
	v_cndmask_b32_e32 v0, v0, v9, vcc
	v_cvt_pk_f16_f32 v1, v1, v0
	v_cvt_pk_f16_f32 v0, v2, v3
	v_cvt_pk_f16_f32 v3, v8, v10
	v_cvt_pk_f16_f32 v2, v6, v7
	global_store_dwordx4 v[4:5], v[0:3], off offset:64
	s_nop 1
	v_accvgpr_read_b32 v0, a12
	v_add_f32_e32 v0, v0, v58
	v_add_f32_e32 v1, 1.0, v0
	v_cndmask_b32_e32 v2, v0, v1, vcc
	v_mul_f32_e32 v0, 0x3fb8aa3b, v0
	v_exp_f32_e32 v6, v0
	v_accvgpr_read_b32 v0, a13
	v_add_f32_e32 v0, v0, v56
	v_add_f32_e32 v1, 1.0, v0
	v_cndmask_b32_e32 v3, v0, v1, vcc
	v_mul_f32_e32 v0, 0x3fb8aa3b, v0
	v_exp_f32_e32 v7, v0
	v_accvgpr_read_b32 v0, a14
	v_add_f32_e32 v0, v0, v60
	v_add_f32_e32 v1, 1.0, v0
	v_cndmask_b32_e32 v1, v0, v1, vcc
	v_mul_f32_e32 v0, 0x3fb8aa3b, v0
	v_exp_f32_e32 v8, v0
	v_accvgpr_read_b32 v0, a15
	v_add_f32_e32 v0, v0, v59
	v_mul_f32_e32 v10, 0x3fb8aa3b, v0
	v_exp_f32_e32 v10, v10
	v_add_f32_e32 v9, 1.0, v0
	v_cndmask_b32_e32 v0, v0, v9, vcc
	v_cvt_pk_f16_f32 v1, v1, v0
	v_cvt_pk_f16_f32 v0, v2, v3
	v_cvt_pk_f16_f32 v3, v8, v10
	v_cvt_pk_f16_f32 v2, v6, v7
	global_store_dwordx4 v[4:5], v[0:3], off offset:96
	s_endpgm

	.amdhsa_kernel _Z11prep_kernelPKfS0_S0_S0_S0_S0_Ph
		.amdhsa_group_segment_fixed_size 4096
		.amdhsa_private_segment_fixed_size 0
		.amdhsa_kernarg_size 56
		.amdhsa_user_sgpr_count 2
		.amdhsa_user_sgpr_dispatch_ptr 0
		.amdhsa_user_sgpr_queue_ptr 0
		.amdhsa_user_sgpr_kernarg_segment_ptr 1
		.amdhsa_user_sgpr_dispatch_id 0
		.amdhsa_user_sgpr_kernarg_preload_length 0
		.amdhsa_user_sgpr_kernarg_preload_offset 0
		.amdhsa_user_sgpr_private_segment_size 0
		.amdhsa_uses_dynamic_stack 0
		.amdhsa_enable_private_segment 0
		.amdhsa_system_sgpr_workgroup_id_x 1
		.amdhsa_system_sgpr_workgroup_id_y 0
		.amdhsa_system_sgpr_workgroup_id_z 0
		.amdhsa_system_sgpr_workgroup_info 0
		.amdhsa_system_vgpr_workitem_id 0
		.amdhsa_next_free_vgpr 112
		.amdhsa_next_free_sgpr 14
		.amdhsa_accum_offset 96
		.amdhsa_reserve_vcc 1
		.amdhsa_float_round_mode_32 0
		.amdhsa_float_round_mode_16_64 0
		.amdhsa_float_denorm_mode_32 3
		.amdhsa_float_denorm_mode_16_64 3
		.amdhsa_dx10_clamp 1
		.amdhsa_ieee_mode 1
		.amdhsa_fp16_overflow 0
		.amdhsa_tg_split 0
		.amdhsa_exception_fp_ieee_invalid_op 0
		.amdhsa_exception_fp_denorm_src 0
		.amdhsa_exception_fp_ieee_div_zero 0
		.amdhsa_exception_fp_ieee_overflow 0
		.amdhsa_exception_fp_ieee_underflow 0
		.amdhsa_exception_fp_ieee_inexact 0
		.amdhsa_exception_int_div_zero 0
	.end_amdhsa_kernel

amdhsa.kernels:
  - .agpr_count:     16
    .args:
      - .actual_access:  read_only
        .address_space:  global
        .offset:         0
        .size:           8
        .value_kind:     global_buffer
      - .actual_access:  read_only
        .address_space:  global
        .offset:         8
        .size:           8
        .value_kind:     global_buffer
      - .actual_access:  read_only
        .address_space:  global
        .offset:         16
        .size:           8
        .value_kind:     global_buffer
      - .actual_access:  read_only
        .address_space:  global
        .offset:         24
        .size:           8
        .value_kind:     global_buffer
      - .actual_access:  read_only
        .address_space:  global
        .offset:         32
        .size:           8
        .value_kind:     global_buffer
      - .actual_access:  read_only
        .address_space:  global
        .offset:         40
        .size:           8
        .value_kind:     global_buffer
      - .actual_access:  write_only
        .address_space:  global
        .offset:         48
        .size:           8
        .value_kind:     global_buffer
    .group_segment_fixed_size: 4096
    .kernarg_segment_align: 8
    .kernarg_segment_size: 56
    .language:       OpenCL C
    .language_version:
      - 2
      - 0
    .max_flat_workgroup_size: 256
    .name:           _Z11prep_kernelPKfS0_S0_S0_S0_S0_Ph
    .private_segment_fixed_size: 0
    .sgpr_count:     20
    .sgpr_spill_count: 0
    .symbol:         _Z11prep_kernelPKfS0_S0_S0_S0_S0_Ph.kd
    .uniform_work_group_size: 1
    .uses_dynamic_stack: false
    .vgpr_count:     112
    .vgpr_spill_count: 0
    .wavefront_size: 64
  - .agpr_count:     0
    .args:
      - .actual_access:  read_only
        .address_space:  global
        .offset:         0
        .size:           8
        .value_kind:     global_buffer
      - .actual_access:  read_only
        .address_space:  global
        .offset:         8
        .size:           8
        .value_kind:     global_buffer
      - .actual_access:  write_only
        .address_space:  global
        .offset:         16
        .size:           8
        .value_kind:     global_buffer
    .group_segment_fixed_size: 108544
    .kernarg_segment_align: 8
    .kernarg_segment_size: 24
    .language:       OpenCL C
    .language_version:
      - 2
      - 0
    .max_flat_workgroup_size: 512
    .name:           _Z11main_kernelPKhPKfPf
    .private_segment_fixed_size: 0
    .sgpr_count:     66
    .sgpr_spill_count: 0
    .symbol:         _Z11main_kernelPKhPKfPf.kd
    .uniform_work_group_size: 1
    .uses_dynamic_stack: false
    .vgpr_count:     256
    .vgpr_spill_count: 0
    .wavefront_size: 64
